# F4: ride-along W_out blocks load all 8 pieces up front; attention prologue csum preload; split K/V prefetch with staggered groups
# baseline (speedup 1.0000x reference)
.LBB2_5:
	s_or_b64 exec, exec, s[4:5]
	s_load_dwordx2 s[38:39], s[0:1], 0x40
	v_and_b32_e32 v87, 63, v0
	v_cmp_gt_u32_e64 s[4:5], 64, v0
	s_and_saveexec_b64 s[44:45], s[4:5]
	s_cbranch_execz .LBB2_9
	s_load_dwordx4 s[4:7], s[0:1], 0x18
	s_load_dwordx2 s[56:57], s[0:1], 0x28
	v_or_b32_e32 v2, s8, v87
	v_mov_b32_e32 v3, 0
	v_lshlrev_b64 v[6:7], 5, v[2:3]
	v_mov_b32_e32 v2, 0
	s_waitcnt lgkmcnt(0)
	v_lshl_add_u64 v[4:5], s[4:5], 0, v[6:7]
	global_load_dwordx4 v[42:45], v[4:5], off
	global_load_dwordx2 v[54:55], v[4:5], off offset:16
	v_lshl_add_u64 v[12:13], s[6:7], 0, v[6:7]
	global_load_dwordx2 v[10:11], v[12:13], off offset:16
	global_load_dwordx4 v[6:9], v[12:13], off
	s_mul_i32 s58, s10, 0x600
	s_add_u32 s56, s56, s58
	s_addc_u32 s57, s57, 0
	v_min_u32_e32 v99, 20, v87
	v_lshlrev_b32_e32 v99, 2, v99
	global_load_dword v100, v99, s[56:57]
	global_load_dword v101, v99, s[56:57] offset:96
	global_load_dword v102, v99, s[56:57] offset:192
	global_load_dword v103, v99, s[56:57] offset:288
	global_load_dword v104, v99, s[56:57] offset:384
	global_load_dword v105, v99, s[56:57] offset:480
	global_load_dword v106, v99, s[56:57] offset:576
	global_load_dword v107, v99, s[56:57] offset:672
	global_load_dword v108, v99, s[56:57] offset:768
	global_load_dword v109, v99, s[56:57] offset:864
	global_load_dword v110, v99, s[56:57] offset:960
	global_load_dword v111, v99, s[56:57] offset:1056
	global_load_dword v112, v99, s[56:57] offset:1152
	global_load_dword v113, v99, s[56:57] offset:1248
	global_load_dword v114, v99, s[56:57] offset:1344
	s_nop 1
	v_mov_b32_e32 v5, 0
	v_cmp_gt_u32_e64 s[4:5], 21, v87
	s_waitcnt vmcnt(0)
	v_mul_f32_e32 v12, v42, v42
	v_mul_f32_e32 v13, v42, v43
	v_mul_f32_e32 v40, v42, v44
	v_mul_f32_e32 v41, v42, v45
	v_mul_f32_e32 v52, v42, v54
	v_mul_f32_e32 v53, v42, v55
	v_mul_f32_e32 v25, v43, v43
	v_mul_f32_e32 v38, v43, v44
	v_mul_f32_e32 v39, v43, v45
	v_mul_f32_e32 v50, v43, v54
	v_mul_f32_e32 v51, v43, v55
	v_mul_f32_e32 v28, v44, v44
	v_mul_f32_e32 v29, v44, v45
	v_mul_f32_e32 v48, v44, v54
	v_mul_f32_e32 v49, v44, v55
	v_mul_f32_e32 v27, v45, v45
	v_mul_f32_e32 v46, v45, v54
	v_mul_f32_e32 v47, v45, v55
	v_mul_f32_e32 v44, v54, v54
	v_mul_f32_e32 v45, v54, v55
	v_mul_f32_e32 v43, v55, v55
	v_add_f32_dpp v12, v12, v12 row_shr:1 row_mask:0xf bank_mask:0xf bound_ctrl:1
	v_add_f32_dpp v13, v13, v13 row_shr:1 row_mask:0xf bank_mask:0xf bound_ctrl:1
	v_add_f32_dpp v40, v40, v40 row_shr:1 row_mask:0xf bank_mask:0xf bound_ctrl:1
	v_add_f32_dpp v41, v41, v41 row_shr:1 row_mask:0xf bank_mask:0xf bound_ctrl:1
	v_add_f32_dpp v52, v52, v52 row_shr:1 row_mask:0xf bank_mask:0xf bound_ctrl:1
	v_add_f32_dpp v53, v53, v53 row_shr:1 row_mask:0xf bank_mask:0xf bound_ctrl:1
	v_add_f32_dpp v25, v25, v25 row_shr:1 row_mask:0xf bank_mask:0xf bound_ctrl:1
	v_add_f32_dpp v38, v38, v38 row_shr:1 row_mask:0xf bank_mask:0xf bound_ctrl:1
	v_add_f32_dpp v39, v39, v39 row_shr:1 row_mask:0xf bank_mask:0xf bound_ctrl:1
	v_add_f32_dpp v50, v50, v50 row_shr:1 row_mask:0xf bank_mask:0xf bound_ctrl:1
	v_add_f32_dpp v51, v51, v51 row_shr:1 row_mask:0xf bank_mask:0xf bound_ctrl:1
	v_add_f32_dpp v28, v28, v28 row_shr:1 row_mask:0xf bank_mask:0xf bound_ctrl:1
	v_add_f32_dpp v29, v29, v29 row_shr:1 row_mask:0xf bank_mask:0xf bound_ctrl:1
	v_add_f32_dpp v48, v48, v48 row_shr:1 row_mask:0xf bank_mask:0xf bound_ctrl:1
	v_add_f32_dpp v49, v49, v49 row_shr:1 row_mask:0xf bank_mask:0xf bound_ctrl:1
	v_add_f32_dpp v27, v27, v27 row_shr:1 row_mask:0xf bank_mask:0xf bound_ctrl:1
	v_add_f32_dpp v46, v46, v46 row_shr:1 row_mask:0xf bank_mask:0xf bound_ctrl:1
	v_add_f32_dpp v47, v47, v47 row_shr:1 row_mask:0xf bank_mask:0xf bound_ctrl:1
	v_add_f32_dpp v44, v44, v44 row_shr:1 row_mask:0xf bank_mask:0xf bound_ctrl:1
	v_add_f32_dpp v45, v45, v45 row_shr:1 row_mask:0xf bank_mask:0xf bound_ctrl:1
	v_add_f32_dpp v43, v43, v43 row_shr:1 row_mask:0xf bank_mask:0xf bound_ctrl:1
	s_nop 0
	v_add_f32_dpp v12, v12, v12 row_shr:2 row_mask:0xf bank_mask:0xf bound_ctrl:1
	v_add_f32_dpp v13, v13, v13 row_shr:2 row_mask:0xf bank_mask:0xf bound_ctrl:1
	v_add_f32_dpp v40, v40, v40 row_shr:2 row_mask:0xf bank_mask:0xf bound_ctrl:1
	v_add_f32_dpp v41, v41, v41 row_shr:2 row_mask:0xf bank_mask:0xf bound_ctrl:1
	v_add_f32_dpp v52, v52, v52 row_shr:2 row_mask:0xf bank_mask:0xf bound_ctrl:1
	v_add_f32_dpp v53, v53, v53 row_shr:2 row_mask:0xf bank_mask:0xf bound_ctrl:1
	v_add_f32_dpp v25, v25, v25 row_shr:2 row_mask:0xf bank_mask:0xf bound_ctrl:1
	v_add_f32_dpp v38, v38, v38 row_shr:2 row_mask:0xf bank_mask:0xf bound_ctrl:1
	v_add_f32_dpp v39, v39, v39 row_shr:2 row_mask:0xf bank_mask:0xf bound_ctrl:1
	v_add_f32_dpp v50, v50, v50 row_shr:2 row_mask:0xf bank_mask:0xf bound_ctrl:1
	v_add_f32_dpp v51, v51, v51 row_shr:2 row_mask:0xf bank_mask:0xf bound_ctrl:1
	v_add_f32_dpp v28, v28, v28 row_shr:2 row_mask:0xf bank_mask:0xf bound_ctrl:1
	v_add_f32_dpp v29, v29, v29 row_shr:2 row_mask:0xf bank_mask:0xf bound_ctrl:1
	v_add_f32_dpp v48, v48, v48 row_shr:2 row_mask:0xf bank_mask:0xf bound_ctrl:1
	v_add_f32_dpp v49, v49, v49 row_shr:2 row_mask:0xf bank_mask:0xf bound_ctrl:1
	v_add_f32_dpp v27, v27, v27 row_shr:2 row_mask:0xf bank_mask:0xf bound_ctrl:1
	v_add_f32_dpp v46, v46, v46 row_shr:2 row_mask:0xf bank_mask:0xf bound_ctrl:1
	v_add_f32_dpp v47, v47, v47 row_shr:2 row_mask:0xf bank_mask:0xf bound_ctrl:1
	v_add_f32_dpp v44, v44, v44 row_shr:2 row_mask:0xf bank_mask:0xf bound_ctrl:1
	v_add_f32_dpp v45, v45, v45 row_shr:2 row_mask:0xf bank_mask:0xf bound_ctrl:1
	v_add_f32_dpp v43, v43, v43 row_shr:2 row_mask:0xf bank_mask:0xf bound_ctrl:1
	s_nop 0
	v_add_f32_dpp v12, v12, v12 row_shr:4 row_mask:0xf bank_mask:0xf bound_ctrl:1
	v_add_f32_dpp v13, v13, v13 row_shr:4 row_mask:0xf bank_mask:0xf bound_ctrl:1
	v_add_f32_dpp v40, v40, v40 row_shr:4 row_mask:0xf bank_mask:0xf bound_ctrl:1
	v_add_f32_dpp v41, v41, v41 row_shr:4 row_mask:0xf bank_mask:0xf bound_ctrl:1
	v_add_f32_dpp v52, v52, v52 row_shr:4 row_mask:0xf bank_mask:0xf bound_ctrl:1
	v_add_f32_dpp v53, v53, v53 row_shr:4 row_mask:0xf bank_mask:0xf bound_ctrl:1
	v_add_f32_dpp v25, v25, v25 row_shr:4 row_mask:0xf bank_mask:0xf bound_ctrl:1
	v_add_f32_dpp v38, v38, v38 row_shr:4 row_mask:0xf bank_mask:0xf bound_ctrl:1
	v_add_f32_dpp v39, v39, v39 row_shr:4 row_mask:0xf bank_mask:0xf bound_ctrl:1
	v_add_f32_dpp v50, v50, v50 row_shr:4 row_mask:0xf bank_mask:0xf bound_ctrl:1
	v_add_f32_dpp v51, v51, v51 row_shr:4 row_mask:0xf bank_mask:0xf bound_ctrl:1
	v_add_f32_dpp v28, v28, v28 row_shr:4 row_mask:0xf bank_mask:0xf bound_ctrl:1
	v_add_f32_dpp v29, v29, v29 row_shr:4 row_mask:0xf bank_mask:0xf bound_ctrl:1
	v_add_f32_dpp v48, v48, v48 row_shr:4 row_mask:0xf bank_mask:0xf bound_ctrl:1
	v_add_f32_dpp v49, v49, v49 row_shr:4 row_mask:0xf bank_mask:0xf bound_ctrl:1
	v_add_f32_dpp v27, v27, v27 row_shr:4 row_mask:0xf bank_mask:0xf bound_ctrl:1
	v_add_f32_dpp v46, v46, v46 row_shr:4 row_mask:0xf bank_mask:0xf bound_ctrl:1
	v_add_f32_dpp v47, v47, v47 row_shr:4 row_mask:0xf bank_mask:0xf bound_ctrl:1
	v_add_f32_dpp v44, v44, v44 row_shr:4 row_mask:0xf bank_mask:0xf bound_ctrl:1
	v_add_f32_dpp v45, v45, v45 row_shr:4 row_mask:0xf bank_mask:0xf bound_ctrl:1
	v_add_f32_dpp v43, v43, v43 row_shr:4 row_mask:0xf bank_mask:0xf bound_ctrl:1
	s_nop 0
	v_add_f32_dpp v12, v12, v12 row_shr:8 row_mask:0xf bank_mask:0xf bound_ctrl:1
	v_add_f32_dpp v13, v13, v13 row_shr:8 row_mask:0xf bank_mask:0xf bound_ctrl:1
	v_add_f32_dpp v40, v40, v40 row_shr:8 row_mask:0xf bank_mask:0xf bound_ctrl:1
	v_add_f32_dpp v41, v41, v41 row_shr:8 row_mask:0xf bank_mask:0xf bound_ctrl:1
	v_add_f32_dpp v52, v52, v52 row_shr:8 row_mask:0xf bank_mask:0xf bound_ctrl:1
	v_add_f32_dpp v53, v53, v53 row_shr:8 row_mask:0xf bank_mask:0xf bound_ctrl:1
	v_add_f32_dpp v25, v25, v25 row_shr:8 row_mask:0xf bank_mask:0xf bound_ctrl:1
	v_add_f32_dpp v38, v38, v38 row_shr:8 row_mask:0xf bank_mask:0xf bound_ctrl:1
	v_add_f32_dpp v39, v39, v39 row_shr:8 row_mask:0xf bank_mask:0xf bound_ctrl:1
	v_add_f32_dpp v50, v50, v50 row_shr:8 row_mask:0xf bank_mask:0xf bound_ctrl:1
	v_add_f32_dpp v51, v51, v51 row_shr:8 row_mask:0xf bank_mask:0xf bound_ctrl:1
	v_add_f32_dpp v28, v28, v28 row_shr:8 row_mask:0xf bank_mask:0xf bound_ctrl:1
	v_add_f32_dpp v29, v29, v29 row_shr:8 row_mask:0xf bank_mask:0xf bound_ctrl:1
	v_add_f32_dpp v48, v48, v48 row_shr:8 row_mask:0xf bank_mask:0xf bound_ctrl:1
	v_add_f32_dpp v49, v49, v49 row_shr:8 row_mask:0xf bank_mask:0xf bound_ctrl:1
	v_add_f32_dpp v27, v27, v27 row_shr:8 row_mask:0xf bank_mask:0xf bound_ctrl:1
	v_add_f32_dpp v46, v46, v46 row_shr:8 row_mask:0xf bank_mask:0xf bound_ctrl:1
	v_add_f32_dpp v47, v47, v47 row_shr:8 row_mask:0xf bank_mask:0xf bound_ctrl:1
	v_add_f32_dpp v44, v44, v44 row_shr:8 row_mask:0xf bank_mask:0xf bound_ctrl:1
	v_add_f32_dpp v45, v45, v45 row_shr:8 row_mask:0xf bank_mask:0xf bound_ctrl:1
	v_add_f32_dpp v43, v43, v43 row_shr:8 row_mask:0xf bank_mask:0xf bound_ctrl:1
	s_nop 0
	v_add_f32_dpp v12, v12, v12 row_bcast:15 row_mask:0xa bank_mask:0xf
	v_add_f32_dpp v13, v13, v13 row_bcast:15 row_mask:0xa bank_mask:0xf
	v_add_f32_dpp v40, v40, v40 row_bcast:15 row_mask:0xa bank_mask:0xf
	v_add_f32_dpp v41, v41, v41 row_bcast:15 row_mask:0xa bank_mask:0xf
	v_add_f32_dpp v52, v52, v52 row_bcast:15 row_mask:0xa bank_mask:0xf
	v_add_f32_dpp v53, v53, v53 row_bcast:15 row_mask:0xa bank_mask:0xf
	v_add_f32_dpp v25, v25, v25 row_bcast:15 row_mask:0xa bank_mask:0xf
	v_add_f32_dpp v38, v38, v38 row_bcast:15 row_mask:0xa bank_mask:0xf
	v_add_f32_dpp v39, v39, v39 row_bcast:15 row_mask:0xa bank_mask:0xf
	v_add_f32_dpp v50, v50, v50 row_bcast:15 row_mask:0xa bank_mask:0xf
	v_add_f32_dpp v51, v51, v51 row_bcast:15 row_mask:0xa bank_mask:0xf
	v_add_f32_dpp v28, v28, v28 row_bcast:15 row_mask:0xa bank_mask:0xf
	v_add_f32_dpp v29, v29, v29 row_bcast:15 row_mask:0xa bank_mask:0xf
	v_add_f32_dpp v48, v48, v48 row_bcast:15 row_mask:0xa bank_mask:0xf
	v_add_f32_dpp v49, v49, v49 row_bcast:15 row_mask:0xa bank_mask:0xf
	v_add_f32_dpp v27, v27, v27 row_bcast:15 row_mask:0xa bank_mask:0xf
	v_add_f32_dpp v46, v46, v46 row_bcast:15 row_mask:0xa bank_mask:0xf
	v_add_f32_dpp v47, v47, v47 row_bcast:15 row_mask:0xa bank_mask:0xf
	v_add_f32_dpp v44, v44, v44 row_bcast:15 row_mask:0xa bank_mask:0xf
	v_add_f32_dpp v45, v45, v45 row_bcast:15 row_mask:0xa bank_mask:0xf
	v_add_f32_dpp v43, v43, v43 row_bcast:15 row_mask:0xa bank_mask:0xf
	s_nop 0
	v_add_f32_dpp v12, v12, v12 row_bcast:31 row_mask:0xc bank_mask:0xf
	v_add_f32_dpp v13, v13, v13 row_bcast:31 row_mask:0xc bank_mask:0xf
	v_add_f32_dpp v40, v40, v40 row_bcast:31 row_mask:0xc bank_mask:0xf
	v_add_f32_dpp v41, v41, v41 row_bcast:31 row_mask:0xc bank_mask:0xf
	v_add_f32_dpp v52, v52, v52 row_bcast:31 row_mask:0xc bank_mask:0xf
	v_add_f32_dpp v53, v53, v53 row_bcast:31 row_mask:0xc bank_mask:0xf
	v_add_f32_dpp v25, v25, v25 row_bcast:31 row_mask:0xc bank_mask:0xf
	v_add_f32_dpp v38, v38, v38 row_bcast:31 row_mask:0xc bank_mask:0xf
	v_add_f32_dpp v39, v39, v39 row_bcast:31 row_mask:0xc bank_mask:0xf
	v_add_f32_dpp v50, v50, v50 row_bcast:31 row_mask:0xc bank_mask:0xf
	v_add_f32_dpp v51, v51, v51 row_bcast:31 row_mask:0xc bank_mask:0xf
	v_add_f32_dpp v28, v28, v28 row_bcast:31 row_mask:0xc bank_mask:0xf
	v_add_f32_dpp v29, v29, v29 row_bcast:31 row_mask:0xc bank_mask:0xf
	v_add_f32_dpp v48, v48, v48 row_bcast:31 row_mask:0xc bank_mask:0xf
	v_add_f32_dpp v49, v49, v49 row_bcast:31 row_mask:0xc bank_mask:0xf
	v_add_f32_dpp v27, v27, v27 row_bcast:31 row_mask:0xc bank_mask:0xf
	v_add_f32_dpp v46, v46, v46 row_bcast:31 row_mask:0xc bank_mask:0xf
	v_add_f32_dpp v47, v47, v47 row_bcast:31 row_mask:0xc bank_mask:0xf
	v_add_f32_dpp v44, v44, v44 row_bcast:31 row_mask:0xc bank_mask:0xf
	v_add_f32_dpp v45, v45, v45 row_bcast:31 row_mask:0xc bank_mask:0xf
	v_add_f32_dpp v43, v43, v43 row_bcast:31 row_mask:0xc bank_mask:0xf
	s_nop 1
	s_and_saveexec_b64 s[48:49], s[4:5]
	s_cbranch_execz .LBB2_8
	s_waitcnt vmcnt(0)
	v_add_f32_e32 v2, 0, v100
	s_cmp_lg_u32 s52, 0
	s_cselect_b64 s[18:19], -1, 0
	v_cndmask_b32_e64 v2, 0, v2, s[18:19]
	s_cmp_gt_u32 s52, 1
	s_cselect_b64 s[4:5], -1, 0
	v_cndmask_b32_e64 v4, 0, v101, s[4:5]
	v_add_f32_e32 v2, v2, v4
	s_cmp_gt_u32 s52, 2
	s_cselect_b64 s[4:5], -1, 0
	v_cndmask_b32_e64 v4, 0, v102, s[4:5]
	v_add_f32_e32 v2, v2, v4
	s_cmp_gt_u32 s52, 3
	s_cselect_b64 s[4:5], -1, 0
	v_cndmask_b32_e64 v4, 0, v103, s[4:5]
	v_add_f32_e32 v2, v2, v4
	s_cmp_gt_u32 s52, 4
	s_cselect_b64 s[4:5], -1, 0
	v_cndmask_b32_e64 v4, 0, v104, s[4:5]
	v_add_f32_e32 v2, v2, v4
	s_cmp_gt_u32 s52, 5
	s_cselect_b64 s[4:5], -1, 0
	v_cndmask_b32_e64 v4, 0, v105, s[4:5]
	v_add_f32_e32 v2, v2, v4
	s_cmp_gt_u32 s52, 6
	s_cselect_b64 s[4:5], -1, 0
	v_cndmask_b32_e64 v4, 0, v106, s[4:5]
	v_add_f32_e32 v2, v2, v4
	s_cmp_gt_u32 s52, 7
	s_cselect_b64 s[4:5], -1, 0
	v_cndmask_b32_e64 v4, 0, v107, s[4:5]
	v_add_f32_e32 v2, v2, v4
	s_cmp_gt_u32 s52, 8
	s_cselect_b64 s[4:5], -1, 0
	v_cndmask_b32_e64 v4, 0, v108, s[4:5]
	v_add_f32_e32 v2, v2, v4
	s_cmp_gt_u32 s52, 9
	s_cselect_b64 s[4:5], -1, 0
	v_cndmask_b32_e64 v4, 0, v109, s[4:5]
	v_add_f32_e32 v2, v2, v4
	s_cmp_gt_u32 s52, 10
	s_cselect_b64 s[4:5], -1, 0
	v_cndmask_b32_e64 v4, 0, v110, s[4:5]
	v_add_f32_e32 v2, v2, v4
	s_cmp_gt_u32 s52, 11
	s_cselect_b64 s[4:5], -1, 0
	v_cndmask_b32_e64 v4, 0, v111, s[4:5]
	v_add_f32_e32 v2, v2, v4
	s_cmp_gt_u32 s52, 12
	s_cselect_b64 s[4:5], -1, 0
	v_cndmask_b32_e64 v4, 0, v112, s[4:5]
	v_add_f32_e32 v2, v2, v4
	s_cmp_gt_u32 s52, 13
	s_cselect_b64 s[4:5], -1, 0
	v_cndmask_b32_e64 v4, 0, v113, s[4:5]
	v_add_f32_e32 v2, v2, v4
	s_cmp_gt_u32 s52, 14
	s_cselect_b64 s[4:5], -1, 0
	v_cndmask_b32_e64 v4, 0, v114, s[4:5]
	v_add_f32_e32 v2, v2, v4

.LBB2_18:
	s_or_b64 exec, exec, s[4:5]
	s_add_i32 s4, s52, 2
	s_lshr_b32 s49, s4, 1
	v_or_b32_e32 v99, 4, v89
	s_mov_b32 s48, 1
	s_cmp_eq_u32 s49, 1
	s_cbranch_scc1 .LBB2_32
	v_or_b32_e32 v1, s33, v37
	v_cmp_gt_u32_e64 s[36:37], v37, v31
	v_cmp_lt_u32_e64 s[4:5], v37, v31
	v_or_b32_e32 v31, 2, v1
	v_cmp_gt_u32_e64 s[6:7], v31, v35
	v_or_b32_e32 v31, 3, v1
	v_cmp_gt_u32_e64 s[8:9], v31, v35
	v_or_b32_e32 v31, 16, v1
	v_cmp_gt_u32_e64 s[10:11], v31, v35
	v_or_b32_e32 v31, 17, v1
	v_cmp_gt_u32_e64 s[12:13], v31, v35
	v_or_b32_e32 v31, 18, v1
	v_cmp_gt_u32_e64 s[14:15], v31, v35
	v_or_b32_e32 v31, 19, v1
	v_cmp_gt_u32_e64 s[16:17], v31, v35
	v_or_b32_e32 v31, 32, v1
	v_cmp_gt_u32_e64 s[18:19], v31, v35
	v_or_b32_e32 v31, 33, v1
	v_cmp_gt_u32_e64 s[20:21], v31, v35
	v_or_b32_e32 v31, 34, v1
	v_cmp_gt_u32_e64 s[22:23], v31, v35
	v_or_b32_e32 v31, 35, v1
	v_cmp_gt_u32_e64 s[24:25], v31, v35
	v_or_b32_e32 v31, 48, v1
	v_cmp_gt_u32_e64 s[26:27], v31, v35
	v_or_b32_e32 v31, 49, v1
	v_cmp_gt_u32_e64 s[28:29], v31, v35
	v_or_b32_e32 v31, 50, v1
	v_or_b32_e32 v1, 51, v1
	v_cmp_gt_u32_e64 s[34:35], v1, v35
	v_mov_b32_e32 v1, 0x100
	v_lshl_or_b32 v72, v88, 6, v1
	v_mov_b32_e32 v1, 0x4000
	v_lshl_or_b32 v70, v88, 12, v1
	v_mov_b32_e32 v1, 0x2000
	s_mov_b32 s44, 0x8000
	v_lshl_or_b32 v74, v88, 11, v1
	v_lshlrev_b32_e32 v78, 1, v30
	s_mov_b32 s45, 0x5040100
	v_xor_b32_e32 v1, 0x8000, v5
	v_xor_b32_sdwa v30, s44, v5 dst_sel:DWORD dst_unused:UNUSED_PAD src0_sel:DWORD src1_sel:WORD_1
	v_lshlrev_b32_e32 v101, 6, v33
	v_perm_b32 v33, v30, v1, s45
	v_xor_b32_e32 v1, 0x8000, v4
	v_xor_b32_sdwa v30, s44, v4 dst_sel:DWORD dst_unused:UNUSED_PAD src0_sel:DWORD src1_sel:WORD_1
	v_lshlrev_b32_e32 v76, 1, v32
	v_perm_b32 v32, v30, v1, s45
	v_xor_b32_e32 v1, 0x8000, v3
	v_xor_b32_sdwa v30, s44, v3 dst_sel:DWORD dst_unused:UNUSED_PAD src0_sel:DWORD src1_sel:WORD_1
	v_cmp_gt_u32_e64 s[30:31], v31, v35
	v_perm_b32 v31, v30, v1, s45
	v_xor_b32_e32 v1, 0x8000, v2
	v_xor_b32_sdwa v30, s44, v2 dst_sel:DWORD dst_unused:UNUSED_PAD src0_sel:DWORD src1_sel:WORD_1
	v_lshlrev_b32_e32 v100, 1, v88
	v_mov_b32_e32 v71, 0
	v_lshlrev_b32_e32 v102, 7, v40
	v_lshlrev_b32_e32 v103, 6, v40
	v_lshlrev_b32_e32 v104, 7, v39
	v_lshlrev_b32_e32 v105, 6, v39
	v_lshlrev_b32_e32 v106, 7, v38
	v_lshlrev_b32_e32 v107, 6, v38
	s_movk_i32 s50, 0x5000
	v_lshlrev_b32_e32 v80, 1, v36
	v_lshlrev_b32_e32 v82, 1, v34
	s_mov_b32 s51, 0xff800000
	s_mov_b32 s53, 0x41700000
	v_perm_b32 v30, v30, v1, s45
	v_mov_b32_e32 v108, 0xff800000
	v_readfirstlane_b32 s58, v88
	v_readfirstlane_b32 s61, v92
	s_waitcnt lgkmcnt(0)
	s_lshl_b32 s61, s61, 1
	s_mul_i32 s59, s58, 0xa000
	s_add_u32 s61, s61, s59
	s_cmp_eq_u32 s58, 0
	s_cbranch_scc1 .Lattn_g0_entry
	s_barrier
.Lattn_g0_entry:
.LBB2_20:
	s_lshl_b32 s59, s48, 1
	s_add_u32 s59, s59, s58
	s_add_u32 s60, s59, 2
	s_and_b32 s62, s48, 1
	s_mul_i32 s63, s62, 0x5000
	s_add_u32 s63, s63, s61
	s_xor_b32 s62, s62, 1
	s_mul_i32 s62, s62, 0x5000
	s_add_u32 s62, s62, s61
	v_add_u32_e32 v109, 2, v50
	s_cmp_gt_u32 s60, s52
	s_cbranch_scc1 .Lattn_top_w0
	s_cmp_lt_u32 s48, 3
	s_cbranch_scc1 .Lattn_top_w0
	s_waitcnt vmcnt(5)
	s_branch .Lattn_top_wd

.Lattn_top_wd:
	s_barrier
	s_cmp_gt_u32 s60, s52
	s_cbranch_scc1 .Lattn_top_noissue
	s_add_u32 m0, s62, 0x2000
	v_lshl_add_u32 v34, v72, 1, v78
	global_load_lds_dwordx4 v34, s[42:43]
	s_add_u32 m0, s62, 0x3000
	v_lshl_add_u32 v35, v72, 1, v82
	global_load_lds_dwordx4 v35, s[42:43]
	s_cmp_lg_u32 s48, 1
	s_cbranch_scc1 .Lattn_top_noissue
	s_mov_b32 m0, s62
	v_lshl_add_u32 v36, v70, 1, v76
	global_load_lds_dwordx4 v36, s[40:41]
	s_add_u32 m0, s62, 0x1000
	v_lshl_add_u32 v37, v70, 1, v80
	global_load_lds_dwordx4 v37, s[40:41]
	v_mov_b32_e32 v75, 0
	s_add_u32 m0, s62, 0x4000
	v_lshl_add_u64 v[38:39], v[74:75], 1, v[66:67]
	global_load_lds_dwordx4 v[38:39], off
.Lattn_top_noissue:
	v_cmp_ge_u32_e32 vcc, s52, v50
	s_and_saveexec_b64 s[44:45], vcc
	s_cbranch_execz .Lattn_skip_mid
	v_and_or_b32 v1, s48, 1, v100
	v_mul_u32_u24_e32 v46, 0x5000, v1
	v_or_b32_e32 v42, v46, v97
	v_add_u32_e32 v75, v42, v94
	ds_read_b128 v[34:37], v75
	v_add_u32_e32 v73, v42, v95
	ds_read_b128 v[42:45], v73
	v_sub_f32_e32 v38, 0x41000000, v69
	v_or_b32_e32 v47, v46, v96
	v_mov_b32_e32 v39, v38
	v_mov_b32_e32 v40, v38
	v_mov_b32_e32 v41, v38
	v_add_u32_e32 v48, v47, v101
	ds_read_b128 v[52:55], v48 offset:16384
	s_waitcnt lgkmcnt(0)
	v_mfma_f32_16x16x32_f16 v[34:37], v[34:37], v[6:9], v[38:41]
	v_or_b32_e32 v46, v46, v102
	v_cmp_eq_u32_e32 vcc, s52, v50
	v_mfma_f32_16x16x32_f16 v[34:37], v[42:45], v[10:13], v[34:37]
	v_add_u32_e32 v42, v46, v94
	ds_read_b128 v[42:45], v42
	v_add_u32_e32 v46, v46, v95
	v_mfma_f32_16x16x32_f16 v[56:59], v[52:55], v[2:5], v[34:37]
	v_mfma_f32_16x16x32_f16 v[34:37], v[52:55], v[30:33], v[34:37]
	ds_read_b128 v[52:55], v46
	v_add_u32_e32 v46, v47, v103
	ds_read_b128 v[60:63], v46 offset:16384
	s_waitcnt lgkmcnt(0)
	v_mfma_f32_16x16x32_f16 v[42:45], v[42:45], v[6:9], v[38:41]
	v_mad_u32_u24 v46, v1, s50, v104
	v_add_u32_e32 v48, v46, v94
	ds_read_b128 v[110:113], v48
	v_mfma_f32_16x16x32_f16 v[42:45], v[52:55], v[10:13], v[42:45]
	v_add_u32_e32 v46, v46, v95
	v_med3_f32 v34, v56, v34, v98
	v_med3_f32 v36, v58, v36, v98
	v_mfma_f32_16x16x32_f16 v[52:55], v[60:63], v[2:5], v[42:45]
	v_mfma_f32_16x16x32_f16 v[42:45], v[60:63], v[30:33], v[42:45]
	ds_read_b128 v[60:63], v46
	v_add_u32_e32 v46, v47, v105
	ds_read_b128 v[114:117], v46 offset:16384
	s_waitcnt lgkmcnt(0)
	v_mfma_f32_16x16x32_f16 v[110:113], v[110:113], v[6:9], v[38:41]
	v_mad_u32_u24 v46, v1, s50, v106
	v_add_u32_e32 v1, v46, v94
	v_mfma_f32_16x16x32_f16 v[60:63], v[60:63], v[10:13], v[110:113]
	s_nop 4
	ds_read_b128 v[110:113], v1
	v_med3_f32 v1, v57, v35, v98
	v_add_u32_e32 v35, v46, v95
	ds_read_b128 v[122:125], v35
	v_add_u32_e32 v35, v47, v107
	v_mfma_f32_16x16x32_f16 v[118:121], v[114:117], v[2:5], v[60:63]
	v_mfma_f32_16x16x32_f16 v[60:63], v[114:117], v[30:33], v[60:63]
	ds_read_b128 v[114:117], v35 offset:16384
	v_med3_f32 v35, v59, v37, v98
	v_med3_f32 v37, v53, v43, v98
	s_waitcnt lgkmcnt(0)
	v_mfma_f32_16x16x32_f16 v[110:113], v[110:113], v[6:9], v[38:41]
	v_mfma_f32_16x16x32_f16 v[56:59], v[122:125], v[10:13], v[110:113]
	s_nop 1
	v_med3_f32 v38, v52, v42, v98
	v_med3_f32 v40, v54, v44, v98
	v_med3_f32 v39, v55, v45, v98
	v_mfma_f32_16x16x32_f16 v[52:55], v[114:117], v[2:5], v[56:59]
	v_med3_f32 v42, v118, v60, v98
	v_med3_f32 v41, v119, v61, v98
	v_med3_f32 v44, v120, v62, v98
	v_mfma_f32_16x16x32_f16 v[56:59], v[114:117], v[30:33], v[56:59]
	v_med3_f32 v43, v121, v63, v98
	s_nop 6
	v_med3_f32 v46, v52, v56, v98
	v_med3_f32 v45, v53, v57, v98
	v_med3_f32 v48, v54, v58, v98
	v_med3_f32 v47, v55, v59, v98
	s_and_saveexec_b64 s[46:47], vcc
	s_cbranch_execz .LBB2_25
	v_mov_b32_e32 v50, s51
	v_cndmask_b32_e64 v50, v34, v50, s[36:37]
	v_cndmask_b32_e64 v34, v50, v34, s[4:5]
	v_mov_b32_e32 v50, s51
	v_cndmask_b32_e64 v1, v108, v1, s[4:5]
	v_cndmask_b32_e64 v36, v36, v108, s[6:7]
	v_cndmask_b32_e64 v35, v35, v108, s[8:9]
	v_cndmask_b32_e64 v38, v38, v50, s[10:11]
	v_cndmask_b32_e64 v37, v37, v108, s[12:13]
	v_cndmask_b32_e64 v40, v40, v108, s[14:15]
	v_cndmask_b32_e64 v39, v39, v108, s[16:17]
	v_cndmask_b32_e64 v42, v42, v50, s[18:19]
	v_cndmask_b32_e64 v41, v41, v108, s[20:21]
	v_cndmask_b32_e64 v44, v44, v108, s[22:23]
	v_cndmask_b32_e64 v43, v43, v108, s[24:25]
	v_cndmask_b32_e64 v46, v46, v50, s[26:27]
	v_cndmask_b32_e64 v45, v45, v108, s[28:29]
	v_cndmask_b32_e64 v48, v48, v108, s[30:31]
	v_cndmask_b32_e64 v47, v47, v108, s[34:35]
.LBB2_25:
	s_or_b64 exec, exec, s[46:47]
	s_cmp_gt_u32 s60, s52
	s_cbranch_scc1 .Lattn_mid_w0
	s_waitcnt vmcnt(5)
	s_branch .Lattn_mid_wd

.Lattn_mid_wd:
	s_barrier
	s_add_u32 s59, s59, 4
	s_cmp_gt_u32 s59, s52
	s_cbranch_scc1 .Lattn_mid_noissue
	s_mov_b32 m0, s63
	v_lshl_add_u32 v52, v70, 1, v76
	v_add_u32_e32 v52, 0x4000, v52
	global_load_lds_dwordx4 v52, s[40:41]
	s_add_u32 m0, s63, 0x1000
	v_lshl_add_u32 v53, v70, 1, v80
	v_add_u32_e32 v53, 0x4000, v53
	global_load_lds_dwordx4 v53, s[40:41]
	v_add_u32_e32 v54, 0x1000, v74
	v_mov_b32_e32 v55, 0
	s_add_u32 m0, s63, 0x4000
	v_lshl_add_u64 v[54:55], v[54:55], 1, v[66:67]
	global_load_lds_dwordx4 v[54:55], off
.Lattn_mid_noissue:
	v_max3_f32 v50, v34, v1, v36
	v_max_f32_e32 v51, v47, v47
	v_max3_f32 v50, v50, v35, v38
	s_nop 0
	v_max3_f32 v50, v50, v37, v40
	s_nop 0
	v_max3_f32 v50, v50, v39, v42
	s_nop 0
	v_max3_f32 v50, v50, v41, v44
	s_nop 0
	v_max3_f32 v50, v50, v43, v46
	s_nop 0
	v_max3_f32 v50, v50, v45, v48
	s_nop 0
	v_max_f32_e32 v50, v50, v50
	v_max_f32_e32 v50, v50, v51
	v_mov_b32_e32 v51, v50
	s_nop 1
	v_permlane16_swap_b32_e32 v50, v51
	v_max_f32 v50, v50, v51
	s_nop 0
	v_mov_b32_e32 v51, v50
	s_nop 1
	v_permlane32_swap_b32_e32 v50, v51
	v_max_f32 v50, v50, v51
	s_nop 0
	v_cmp_lt_f32_e32 vcc, s53, v50
	s_cbranch_vccz .Lattn_fast
	v_add_f32_e32 v50, 0xc1000000, v50
	v_cndmask_b32_e32 v77, 0, v50, vcc
	v_exp_f32_e64 v84, -v77
	v_sub_f32_e32 v122, v34, v77
	v_sub_f32_e32 v121, v1, v77
	v_sub_f32_e32 v120, v36, v77
	v_pk_mul_f32 v[52:53], v[84:85], v[28:29] op_sel_hi:[0,1]
	v_pk_mul_f32 v[50:51], v[84:85], v[26:27] op_sel_hi:[0,1]
	v_pk_mul_f32 v[56:57], v[84:85], v[24:25] op_sel_hi:[0,1]
	v_pk_mul_f32 v[54:55], v[84:85], v[22:23] op_sel_hi:[0,1]
	v_pk_mul_f32 v[64:65], v[84:85], v[20:21] op_sel_hi:[0,1]
	v_pk_mul_f32 v[62:63], v[84:85], v[18:19] op_sel_hi:[0,1]
	v_pk_mul_f32 v[60:61], v[84:85], v[16:17] op_sel_hi:[0,1]
	v_pk_mul_f32 v[58:59], v[84:85], v[14:15] op_sel_hi:[0,1]
	v_sub_f32_e32 v119, v35, v77
	v_sub_f32_e32 v118, v38, v77
	v_sub_f32_e32 v114, v37, v77
	v_sub_f32_e32 v117, v40, v77
	v_sub_f32_e32 v116, v39, v77
	v_sub_f32_e32 v115, v42, v77
	v_sub_f32_e32 v113, v41, v77
	v_sub_f32_e32 v112, v44, v77
	v_sub_f32_e32 v110, v43, v77
	v_sub_f32_e32 v83, v46, v77
	v_sub_f32_e32 v79, v45, v77
	v_sub_f32_e32 v111, v48, v77
	v_sub_f32_e32 v81, v47, v77
	v_mul_f32_e32 v84, v68, v84
	s_cbranch_execnz .LBB2_28

.Lattn_loop_exit:
	s_cmp_lg_u32 s58, 0
	s_cbranch_scc1 .LBB2_32
	s_barrier

.LBB2_37:
	s_load_dwordx4 s[4:7], s[0:1], 0x48
	v_lshl_or_b32 v14, s2, 11, v0
	v_mov_b32_e32 v9, 0
	v_add_u32_e32 v8, 0xfff00000, v14
	v_lshlrev_b64 v[0:1], 5, v[8:9]
	v_lshlrev_b64 v[2:3], 4, v[8:9]
	s_mov_b64 s[8:9], 0x4000
	s_mov_b64 s[10:11], 0x2000
	s_waitcnt lgkmcnt(0)
	v_lshl_add_u64 v[10:11], s[4:5], 0, v[0:1]
	v_lshl_add_u64 v[4:5], s[6:7], 0, v[2:3]
	global_load_dwordx4 v[16:19], v[10:11], off nt
	global_load_dwordx4 v[20:23], v[10:11], off offset:16 nt
	v_lshl_add_u64 v[10:11], v[10:11], 0, s[8:9]
	global_load_dwordx4 v[24:27], v[10:11], off nt
	global_load_dwordx4 v[28:31], v[10:11], off offset:16 nt
	v_lshl_add_u64 v[10:11], v[10:11], 0, s[8:9]
	global_load_dwordx4 v[32:35], v[10:11], off nt
	global_load_dwordx4 v[36:39], v[10:11], off offset:16 nt
	v_lshl_add_u64 v[10:11], v[10:11], 0, s[8:9]
	global_load_dwordx4 v[40:43], v[10:11], off nt
	global_load_dwordx4 v[44:47], v[10:11], off offset:16 nt
	s_waitcnt vmcnt(6)
	v_cvt_pk_f16_f32 v48, v16, v17
	v_cvt_pk_f16_f32 v49, v18, v19
	v_cvt_pk_f16_f32 v50, v20, v21
	v_cvt_pk_f16_f32 v51, v22, v23
	global_store_dwordx4 v[4:5], v[48:51], off sc1
	v_lshl_add_u64 v[4:5], v[4:5], 0, s[10:11]
	s_waitcnt vmcnt(5)
	v_cvt_pk_f16_f32 v52, v24, v25
	v_cvt_pk_f16_f32 v53, v26, v27
	v_cvt_pk_f16_f32 v54, v28, v29
	v_cvt_pk_f16_f32 v55, v30, v31
	global_store_dwordx4 v[4:5], v[52:55], off sc1
	v_lshl_add_u64 v[4:5], v[4:5], 0, s[10:11]
	s_waitcnt vmcnt(4)
	v_cvt_pk_f16_f32 v56, v32, v33
	v_cvt_pk_f16_f32 v57, v34, v35
	v_cvt_pk_f16_f32 v58, v36, v37
	v_cvt_pk_f16_f32 v59, v38, v39
	global_store_dwordx4 v[4:5], v[56:59], off sc1
	v_lshl_add_u64 v[4:5], v[4:5], 0, s[10:11]
	s_waitcnt vmcnt(3)
	v_cvt_pk_f16_f32 v60, v40, v41
	v_cvt_pk_f16_f32 v61, v42, v43
	v_cvt_pk_f16_f32 v62, v44, v45
	v_cvt_pk_f16_f32 v63, v46, v47
	global_store_dwordx4 v[4:5], v[60:63], off sc1
	s_nop 1
	s_endpgm

amdhsa.kernels:
  - .agpr_count:     0
    .args:
      - .actual_access:  read_only
        .address_space:  global
        .offset:         0
        .size:           8
        .value_kind:     global_buffer
      - .actual_access:  read_only
        .address_space:  global
        .offset:         8
        .size:           8
        .value_kind:     global_buffer
      - .actual_access:  read_only
        .address_space:  global
        .offset:         16
        .size:           8
        .value_kind:     global_buffer
      - .actual_access:  read_only
        .address_space:  global
        .offset:         24
        .size:           8
        .value_kind:     global_buffer
      - .actual_access:  read_only
        .address_space:  global
        .offset:         32
        .size:           8
        .value_kind:     global_buffer
      - .actual_access:  read_only
        .address_space:  global
        .offset:         40
        .size:           8
        .value_kind:     global_buffer
      - .actual_access:  read_only
        .address_space:  global
        .offset:         48
        .size:           8
        .value_kind:     global_buffer
      - .address_space:  global
        .offset:         56
        .size:           8
        .value_kind:     global_buffer
      - .address_space:  global
        .offset:         64
        .size:           8
        .value_kind:     global_buffer
      - .actual_access:  read_only
        .address_space:  global
        .offset:         72
        .size:           8
        .value_kind:     global_buffer
      - .address_space:  global
        .offset:         80
        .size:           8
        .value_kind:     global_buffer
    .group_segment_fixed_size: 0
    .kernarg_segment_align: 8
    .kernarg_segment_size: 88
    .language:       OpenCL C
    .language_version:
      - 2
      - 0
    .max_flat_workgroup_size: 256
    .name:           _Z11prep_kernelPKfS0_S0_S0_S0_S0_S0_PDF16_S1_S1_S1_
    .private_segment_fixed_size: 0
    .sgpr_count:     23
    .sgpr_spill_count: 0
    .symbol:         _Z11prep_kernelPKfS0_S0_S0_S0_S0_S0_PDF16_S1_S1_S1_.kd
    .uniform_work_group_size: 1
    .uses_dynamic_stack: false
    .vgpr_count:     28
    .vgpr_spill_count: 0
    .wavefront_size: 64
  - .agpr_count:     0
    .args:
      - .offset:         0
        .size:           88
        .value_kind:     by_value
    .group_segment_fixed_size: 163840
    .kernarg_segment_align: 8
    .kernarg_segment_size: 88
    .language:       OpenCL C
    .language_version:
      - 2
      - 0
    .max_flat_workgroup_size: 512
    .name:           _Z12gemm1_kernel6G1Args
    .private_segment_fixed_size: 0
    .sgpr_count:     58
    .sgpr_spill_count: 0
    .symbol:         _Z12gemm1_kernel6G1Args.kd
    .uniform_work_group_size: 1
    .uses_dynamic_stack: false
    .vgpr_count:     240
    .vgpr_spill_count: 0
    .wavefront_size: 64
  - .agpr_count:     0
    .args:
      - .address_space:  global
        .offset:         0
        .size:           8
        .value_kind:     global_buffer
      - .address_space:  global
        .offset:         8
        .size:           8
        .value_kind:     global_buffer
      - .address_space:  global
        .offset:         16
        .size:           8
        .value_kind:     global_buffer
      - .actual_access:  read_only
        .address_space:  global
        .offset:         24
        .size:           8
        .value_kind:     global_buffer
      - .actual_access:  read_only
        .address_space:  global
        .offset:         32
        .size:           8
        .value_kind:     global_buffer
      - .actual_access:  read_only
        .address_space:  global
        .offset:         40
        .size:           8
        .value_kind:     global_buffer
      - .address_space:  global
        .offset:         48
        .size:           8
        .value_kind:     global_buffer
      - .actual_access:  read_only
        .address_space:  global
        .offset:         56
        .size:           8
        .value_kind:     global_buffer
      - .address_space:  global
        .offset:         64
        .size:           8
        .value_kind:     global_buffer
      - .actual_access:  read_only
        .address_space:  global
        .offset:         72
        .size:           8
        .value_kind:     global_buffer
      - .address_space:  global
        .offset:         80
        .size:           8
        .value_kind:     global_buffer
    .group_segment_fixed_size: 81920
    .kernarg_segment_align: 8
    .kernarg_segment_size: 88
    .language:       OpenCL C
    .language_version:
      - 2
      - 0
    .max_flat_workgroup_size: 512
    .name:           _Z11attn_kernelPKDF16_S0_S0_PKfS2_S2_S0_S2_PDF16_S2_S3_
    .private_segment_fixed_size: 0
    .sgpr_count:     70
    .sgpr_spill_count: 0
    .symbol:         _Z11attn_kernelPKDF16_S0_S0_PKfS2_S2_S0_S2_PDF16_S2_S3_.kd
    .uniform_work_group_size: 1
    .uses_dynamic_stack: false
    .vgpr_count:     126
    .vgpr_spill_count: 0
    .wavefront_size: 64
  - .agpr_count:     0
    .args:
      - .address_space:  global
        .offset:         0
        .size:           8
        .value_kind:     global_buffer
      - .address_space:  global
        .offset:         8
        .size:           8
        .value_kind:     global_buffer
      - .actual_access:  read_only
        .address_space:  global
        .offset:         16
        .size:           8
        .value_kind:     global_buffer
      - .actual_access:  write_only
        .address_space:  global
        .offset:         24
        .size:           8
        .value_kind:     global_buffer
    .group_segment_fixed_size: 122880
    .kernarg_segment_align: 8
    .kernarg_segment_size: 32
    .language:       OpenCL C
    .language_version:
      - 2
      - 0
    .max_flat_workgroup_size: 512
    .name:           _Z14outproj_kernelPKDF16_S0_PKfPf
    .private_segment_fixed_size: 0
    .sgpr_count:     31
    .sgpr_spill_count: 0
    .symbol:         _Z14outproj_kernelPKDF16_S0_PKfPf.kd
    .uniform_work_group_size: 1
    .uses_dynamic_stack: false
    .vgpr_count:     132
    .vgpr_spill_count: 0
    .wavefront_size: 64
